# grid barrier: the XCD leader no longer waits for the acknowledgement of its generation-word atomics before leaving the barrier
# speedup vs baseline: 1.0108x; 1.0007x over previous
.LBB0_222:
	s_or_b64 exec, exec, s[2:3]
	s_waitcnt vmcnt(0)
	global_atomic_add v[170:171], v187, off
	s_nop 0
	s_nop 0
